# expert down GEMM: tile's row gates and bias fetched by LDS-DMA at K-loop start into a double-buffered LDS area; the epilogue reads them from LDS instead of starting with 12 global loads and a full vmc
# speedup vs baseline: 1.0015x; 1.0015x over previous
.LBB0_1504:
	s_ashr_i32 s41, s40, 31
	s_lshl_b64 s[10:11], s[40:41], 21
	s_add_u32 s31, s13, s10
	s_addc_u32 s41, s17, s11
	v_readlane_b32 s10, v253, 36
	v_readlane_b32 s11, v253, 37
	s_mov_b32 s46, s10
	s_ashr_i32 s47, s10, 31
	v_writelane_b32 v253, s10, 36
	v_lshl_add_u32 v2, s61, 18, v239
	v_mov_b32_e32 v66, 0
	v_writelane_b32 v253, s11, 37
	s_lshl_b64 s[10:11], s[46:47], 18
	s_add_u32 s10, s31, s10
	s_addc_u32 s11, s41, s11
	s_and_b64 s[46:47], s[8:9], exec
	s_cselect_b32 s41, s11, s45
	s_cselect_b32 s65, s10, s44
	s_add_u32 s66, s44, 0x100
	s_addc_u32 s68, s45, 0
	v_readlane_b32 s44, v253, 42
	v_add_u32_e32 v245, v2, v238
	v_add_u32_e32 v246, v240, v2
	v_add_u32_e32 v212, v241, v2
	v_add_u32_e32 v214, v242, v2
	v_mov_b32_e32 v213, v99
	v_mov_b32_e32 v215, v99
	s_mov_b32 s83, -2
	v_readlane_b32 s45, v253, 43
	v_mov_b32_e32 v67, v66
	v_mov_b32_e32 v68, v66
	v_mov_b32_e32 v69, v66
	v_mov_b32_e32 v70, v66
	v_mov_b32_e32 v71, v66
	v_mov_b32_e32 v72, v66
	v_mov_b32_e32 v73, v66
	v_mov_b32_e32 v74, v66
	v_mov_b32_e32 v75, v66
	v_mov_b32_e32 v76, v66
	v_mov_b32_e32 v77, v66
	v_mov_b32_e32 v78, v66
	v_mov_b32_e32 v79, v66
	v_mov_b32_e32 v80, v66
	v_mov_b32_e32 v81, v66
	v_mov_b32_e32 v82, v66
	v_mov_b32_e32 v83, v66
	v_mov_b32_e32 v84, v66
	v_mov_b32_e32 v85, v66
	v_mov_b32_e32 v86, v66
	v_mov_b32_e32 v87, v66
	v_mov_b32_e32 v88, v66
	v_mov_b32_e32 v89, v66
	v_mov_b32_e32 v90, v66
	v_mov_b32_e32 v91, v66
	v_mov_b32_e32 v92, v66
	v_mov_b32_e32 v93, v66
	v_mov_b32_e32 v94, v66
	v_mov_b32_e32 v95, v66
	v_mov_b32_e32 v96, v66
	v_mov_b32_e32 v97, v66
	v_mov_b32_e32 v124, v66
	v_mov_b32_e32 v125, v66
	v_mov_b32_e32 v126, v66
	v_mov_b32_e32 v127, v66
	v_mov_b32_e32 v132, v66
	v_mov_b32_e32 v133, v66
	v_mov_b32_e32 v134, v66
	v_mov_b32_e32 v135, v66
	v_mov_b32_e32 v140, v66
	v_mov_b32_e32 v141, v66
	v_mov_b32_e32 v142, v66
	v_mov_b32_e32 v143, v66
	v_mov_b32_e32 v144, v66
	v_mov_b32_e32 v145, v66
	v_mov_b32_e32 v146, v66
	v_mov_b32_e32 v147, v66
	v_mov_b32_e32 v148, v66
	v_mov_b32_e32 v149, v66
	v_mov_b32_e32 v150, v66
	v_mov_b32_e32 v151, v66
	v_mov_b32_e32 v152, v66
	v_mov_b32_e32 v153, v66
	v_mov_b32_e32 v154, v66
	v_mov_b32_e32 v155, v66
	v_mov_b32_e32 v156, v66
	v_mov_b32_e32 v157, v66
	v_mov_b32_e32 v158, v66
	v_mov_b32_e32 v159, v66
	v_mov_b32_e32 v160, v66
	v_mov_b32_e32 v161, v66
	v_mov_b32_e32 v162, v66
	v_mov_b32_e32 v163, v66
	v_mov_b32_e32 v100, v66
	v_mov_b32_e32 v101, v66
	v_mov_b32_e32 v102, v66
	v_mov_b32_e32 v103, v66
	v_mov_b32_e32 v104, v66
	v_mov_b32_e32 v105, v66
	v_mov_b32_e32 v106, v66
	v_mov_b32_e32 v107, v66
	v_mov_b32_e32 v108, v66
	v_mov_b32_e32 v109, v66
	v_mov_b32_e32 v110, v66
	v_mov_b32_e32 v111, v66
	v_mov_b32_e32 v112, v66
	v_mov_b32_e32 v113, v66
	v_mov_b32_e32 v114, v66
	v_mov_b32_e32 v115, v66
	v_mov_b32_e32 v116, v66
	v_mov_b32_e32 v117, v66
	v_mov_b32_e32 v118, v66
	v_mov_b32_e32 v119, v66
	v_mov_b32_e32 v120, v66
	v_mov_b32_e32 v121, v66
	v_mov_b32_e32 v122, v66
	v_mov_b32_e32 v123, v66
	v_mov_b32_e32 v128, v66
	v_mov_b32_e32 v129, v66
	v_mov_b32_e32 v130, v66
	v_mov_b32_e32 v131, v66
	v_mov_b32_e32 v136, v66
	v_mov_b32_e32 v137, v66
	v_mov_b32_e32 v138, v66
	v_mov_b32_e32 v139, v66
	v_mov_b32_e32 v164, v66
	v_mov_b32_e32 v165, v66
	v_mov_b32_e32 v166, v66
	v_mov_b32_e32 v167, v66
	v_mov_b32_e32 v168, v66
	v_mov_b32_e32 v169, v66
	v_mov_b32_e32 v170, v66
	v_mov_b32_e32 v171, v66
	v_mov_b32_e32 v172, v66
	v_mov_b32_e32 v173, v66
	v_mov_b32_e32 v174, v66
	v_mov_b32_e32 v175, v66
	v_mov_b32_e32 v176, v66
	v_mov_b32_e32 v177, v66
	v_mov_b32_e32 v178, v66
	v_mov_b32_e32 v179, v66
	v_mov_b32_e32 v180, v66
	v_mov_b32_e32 v181, v66
	v_mov_b32_e32 v182, v66
	v_mov_b32_e32 v183, v66
	v_mov_b32_e32 v184, v66
	v_mov_b32_e32 v185, v66
	v_mov_b32_e32 v186, v66
	v_mov_b32_e32 v187, v66
	v_mov_b32_e32 v188, v66
	v_mov_b32_e32 v189, v66
	v_mov_b32_e32 v190, v66
	v_mov_b32_e32 v191, v66
	v_mov_b32_e32 v192, v66
	v_mov_b32_e32 v193, v66
	v_mov_b32_e32 v194, v66
	v_mov_b32_e32 v195, v66
	s_waitcnt vmcnt(0)
	v_mbcnt_lo_u32_b32 v3, -1, 0
	v_mbcnt_hi_u32_b32 v3, -1, v3
	v_readfirstlane_b32 s100, v0
	v_lshlrev_b32_e32 v3, 2, v3
	s_lshr_b32 s100, s100, 6
	s_and_b32 vcc_lo, s60, 1
	s_lshl_b32 vcc_lo, vcc_lo, 11
	s_add_i32 vcc_lo, vcc_lo, 0x20c00
	s_cmp_gt_u32 s100, 3
	s_cbranch_scc1 .Lg2pf_bias
	s_lshl_b32 vcc_hi, s100, 8
	s_add_i32 m0, vcc_lo, vcc_hi
	s_lshl_b32 s101, s43, 10
	s_add_i32 s101, s101, vcc_hi
	s_add_u32 s100, s70, s101
	s_addc_u32 s101, s71, 0
	s_branch .Lg2pf_go
.Lg2pf_bias:
	s_sub_i32 s100, s100, 4
	s_lshl_b32 vcc_hi, s100, 8
	s_add_i32 m0, vcc_lo, vcc_hi
	s_add_i32 m0, m0, 0x400
	v_readlane_b32 s101, v253, 36
	s_lshl_b32 s100, s42, 13
	s_lshl_b32 s101, s101, 10
	s_add_i32 s101, s101, vcc_hi
	s_add_i32 s101, s101, s100
	s_add_u32 s100, s51, s101
	s_addc_u32 s101, s52, 0
.Lg2pf_go:
	s_nop 0
	global_load_lds_dword v3, s[100:101]
	s_branch .LBB0_1507

.LBB0_1511:
	s_lshl_b32 s31, s43, 8
	v_mov_b32_e32 v2, v237
	v_mov_b32_e32 v3, v201
	s_add_i32 s31, s31, s53
	v_readlane_b32 s44, v253, 36
	s_ashr_i32 s43, s42, 31
	v_add_u32_e32 v34, s31, v3
	s_lshl_b32 s31, s44, 8
	s_or_b32 s31, s31, s12
	s_lshl_b64 s[42:43], s[42:43], 13
	v_lshl_add_u32 v36, v2, 3, s31
	s_add_u32 s42, s51, s42
	v_ashrrev_i32_e32 v37, 31, v36
	v_ashrrev_i32_e32 v35, 31, v34
	s_addc_u32 s43, s52, s43
	s_and_b32 s100, s60, 1
	s_lshl_b32 s100, s100, 11
	s_add_i32 s100, s100, 0x20c00
	s_lshl_b32 s101, s53, 2
	s_add_i32 s101, s101, s100
	v_lshl_add_u32 v18, v3, 2, s101
	s_lshl_b32 s101, s12, 2
	s_add_i32 s101, s101, s100
	s_add_i32 s101, s101, 0x400
	v_lshl_add_u32 v6, v2, 5, s101
	ds_read_b128 v[10:13], v6 offset:16
	ds_read_b128 v[14:17], v6
	ds_read_b128 v[2:5], v6 offset:528
	ds_read_b128 v[6:9], v6 offset:512
	ds_read_b32 v21, v18 offset:704
	ds_read_b32 v20, v18 offset:640
	ds_read_b32 v22, v18 offset:576
	ds_read_b32 v23, v18 offset:512
	ds_read_b32 v24, v18 offset:192
	ds_read_b32 v25, v18 offset:128
	ds_read_b32 v26, v18 offset:64
	ds_read_b32 v18, v18
	v_mov_b32_e32 v46, v99
	v_mov_b32_e32 v47, v99
	v_readlane_b32 s42, v251, 14
	v_lshlrev_b64 v[34:35], 11, v[34:35]
	v_readlane_b32 s43, v251, 15
	s_mov_b32 s31, 0x8000
	v_mov_b32_e32 v48, v99
	v_lshl_add_u64 v[34:35], s[42:43], 0, v[34:35]
	v_lshl_add_u64 v[34:35], v[34:35], 0, v[36:37]
	v_mov_b32_e32 v49, v99
	v_mov_b32_e32 v50, v99
	v_mov_b32_e32 v51, v99
	v_mov_b32_e32 v52, v99
	v_mov_b32_e32 v53, v99
	v_mov_b32_e32 v54, v99
	v_mov_b32_e32 v55, v99
	s_mov_b64 s[42:43], 0x8000
	s_mov_b64 s[46:47], s[36:37]
	v_readlane_b32 s83, v255, 2
	v_readlane_b32 s65, v255, 3
	s_movk_i32 s66, 0x5ff
	v_readlane_b32 s45, v253, 37
	s_waitcnt lgkmcnt(0)
	s_nop 0
	v_mul_f32_e32 v32, 0x41800000, v18
	v_pk_add_f32 v[40:41], v[192:193], v[14:15]
	v_pk_add_f32 v[44:45], v[188:189], v[10:11]
	v_pk_mul_f32 v[40:41], v[40:41], v[32:33] op_sel_hi:[1,0]
	v_pk_mul_f32 v[44:45], v[44:45], v[32:33] op_sel_hi:[1,0]
	v_cvt_pk_fp8_f32 v46, v40, v41
	v_cvt_pk_fp8_f32 v47, v44, v45
	v_pk_add_f32 v[38:39], v[194:195], v[16:17]
	v_pk_add_f32 v[42:43], v[190:191], v[12:13]
	v_pk_mul_f32 v[38:39], v[38:39], v[32:33] op_sel_hi:[1,0]
	v_pk_mul_f32 v[42:43], v[42:43], v[32:33] op_sel_hi:[1,0]
	v_mul_f32_e32 v30, 0x41800000, v26
	v_cvt_pk_fp8_f32 v46, v38, v39 op_sel:[0,0,1]
	v_cvt_pk_fp8_f32 v47, v42, v43 op_sel:[0,0,1]
	v_pk_add_f32 v[38:39], v[184:185], v[14:15]
	v_pk_add_f32 v[42:43], v[180:181], v[10:11]
	v_pk_mul_f32 v[38:39], v[38:39], v[30:31] op_sel_hi:[1,0]
	v_pk_mul_f32 v[42:43], v[42:43], v[30:31] op_sel_hi:[1,0]
	v_mov_b32_e32 v44, v99
	v_mov_b32_e32 v45, v99
	v_cvt_pk_fp8_f32 v44, v38, v39
	v_cvt_pk_fp8_f32 v45, v42, v43
	v_pk_add_f32 v[36:37], v[186:187], v[16:17]
	v_pk_add_f32 v[40:41], v[182:183], v[12:13]
	v_pk_mul_f32 v[36:37], v[36:37], v[30:31] op_sel_hi:[1,0]
	v_pk_mul_f32 v[40:41], v[40:41], v[30:31] op_sel_hi:[1,0]
	v_cvt_pk_fp8_f32 v44, v36, v37 op_sel:[0,0,1]
	v_cvt_pk_fp8_f32 v45, v40, v41 op_sel:[0,0,1]
	v_add_co_u32_e32 v38, vcc, s31, v34
	v_mul_f32_e32 v28, 0x41800000, v25
	s_nop 0
	v_addc_co_u32_e32 v39, vcc, 0, v35, vcc
	global_store_dwordx2 v[38:39], v[44:45], off
	v_pk_add_f32 v[40:41], v[176:177], v[14:15]
	v_pk_add_f32 v[44:45], v[172:173], v[10:11]
	global_store_dwordx2 v[34:35], v[46:47], off
	v_pk_mul_f32 v[40:41], v[40:41], v[28:29] op_sel_hi:[1,0]
	v_pk_mul_f32 v[44:45], v[44:45], v[28:29] op_sel_hi:[1,0]
	v_mov_b32_e32 v46, v99
	v_mov_b32_e32 v47, v99
	v_cvt_pk_fp8_f32 v46, v40, v41
	v_cvt_pk_fp8_f32 v47, v44, v45
	v_pk_add_f32 v[38:39], v[178:179], v[16:17]
	v_pk_add_f32 v[42:43], v[174:175], v[12:13]
	v_pk_mul_f32 v[38:39], v[38:39], v[28:29] op_sel_hi:[1,0]
	v_pk_mul_f32 v[42:43], v[42:43], v[28:29] op_sel_hi:[1,0]
	v_cvt_pk_fp8_f32 v46, v38, v39 op_sel:[0,0,1]
	v_cvt_pk_fp8_f32 v47, v42, v43 op_sel:[0,0,1]
	s_mov_b32 s31, 0x10000
	v_add_co_u32_e32 v40, vcc, s31, v34
	v_mul_f32_e32 v26, 0x41800000, v24
	s_nop 0
	v_addc_co_u32_e32 v41, vcc, 0, v35, vcc
	global_store_dwordx2 v[40:41], v[46:47], off
	v_pk_add_f32 v[42:43], v[168:169], v[14:15]
	v_pk_add_f32 v[46:47], v[164:165], v[10:11]
	v_pk_mul_f32 v[42:43], v[42:43], v[26:27] op_sel_hi:[1,0]
	v_pk_mul_f32 v[46:47], v[46:47], v[26:27] op_sel_hi:[1,0]
	v_cvt_pk_fp8_f32 v48, v42, v43
	v_cvt_pk_fp8_f32 v49, v46, v47
	v_pk_add_f32 v[40:41], v[170:171], v[16:17]
	v_pk_add_f32 v[44:45], v[166:167], v[12:13]
	v_pk_mul_f32 v[40:41], v[40:41], v[26:27] op_sel_hi:[1,0]
	v_pk_mul_f32 v[44:45], v[44:45], v[26:27] op_sel_hi:[1,0]
	v_cvt_pk_fp8_f32 v48, v40, v41 op_sel:[0,0,1]
	v_cvt_pk_fp8_f32 v49, v44, v45 op_sel:[0,0,1]
	s_mov_b32 s31, 0x18000
	v_add_co_u32_e32 v42, vcc, s31, v34
	v_mul_f32_e32 v24, 0x41800000, v23
	s_nop 0
	v_addc_co_u32_e32 v43, vcc, 0, v35, vcc
	global_store_dwordx2 v[42:43], v[48:49], off
	v_pk_add_f32 v[44:45], v[160:161], v[14:15]
	v_pk_add_f32 v[48:49], v[156:157], v[10:11]
	v_pk_mul_f32 v[44:45], v[44:45], v[24:25] op_sel_hi:[1,0]
	v_pk_mul_f32 v[48:49], v[48:49], v[24:25] op_sel_hi:[1,0]
	v_cvt_pk_fp8_f32 v50, v44, v45
	v_cvt_pk_fp8_f32 v51, v48, v49
	v_pk_add_f32 v[42:43], v[162:163], v[16:17]
	v_pk_add_f32 v[46:47], v[158:159], v[12:13]
	v_pk_mul_f32 v[42:43], v[42:43], v[24:25] op_sel_hi:[1,0]
	v_pk_mul_f32 v[46:47], v[46:47], v[24:25] op_sel_hi:[1,0]
	v_cvt_pk_fp8_f32 v50, v42, v43 op_sel:[0,0,1]
	v_cvt_pk_fp8_f32 v51, v46, v47 op_sel:[0,0,1]
	s_mov_b32 s31, 0x40000
	v_add_co_u32_e32 v44, vcc, s31, v34
	v_mul_f32_e32 v22, 0x41800000, v22
	s_nop 0
	v_addc_co_u32_e32 v45, vcc, 0, v35, vcc
	global_store_dwordx2 v[44:45], v[50:51], off
	v_pk_add_f32 v[46:47], v[152:153], v[14:15]
	v_pk_add_f32 v[50:51], v[148:149], v[10:11]
	v_pk_mul_f32 v[46:47], v[46:47], v[22:23] op_sel_hi:[1,0]
	v_pk_mul_f32 v[50:51], v[50:51], v[22:23] op_sel_hi:[1,0]
	v_cvt_pk_fp8_f32 v52, v46, v47
	v_cvt_pk_fp8_f32 v53, v50, v51
	v_pk_add_f32 v[44:45], v[154:155], v[16:17]
	v_pk_add_f32 v[48:49], v[150:151], v[12:13]
	v_pk_mul_f32 v[44:45], v[44:45], v[22:23] op_sel_hi:[1,0]
	v_pk_mul_f32 v[48:49], v[48:49], v[22:23] op_sel_hi:[1,0]
	v_cvt_pk_fp8_f32 v52, v44, v45 op_sel:[0,0,1]
	v_cvt_pk_fp8_f32 v53, v48, v49 op_sel:[0,0,1]
	s_mov_b32 s31, 0x48000
	v_add_co_u32_e32 v46, vcc, s31, v34
	v_mul_f32_e32 v20, 0x41800000, v20
	s_nop 0
	v_addc_co_u32_e32 v47, vcc, 0, v35, vcc
	global_store_dwordx2 v[46:47], v[52:53], off
	v_pk_add_f32 v[48:49], v[144:145], v[14:15]
	v_pk_add_f32 v[52:53], v[140:141], v[10:11]
	v_pk_mul_f32 v[48:49], v[48:49], v[20:21] op_sel_hi:[1,0]
	v_pk_mul_f32 v[52:53], v[52:53], v[20:21] op_sel_hi:[1,0]
	v_cvt_pk_fp8_f32 v54, v48, v49
	v_cvt_pk_fp8_f32 v55, v52, v53
	v_pk_add_f32 v[46:47], v[146:147], v[16:17]
	v_pk_add_f32 v[50:51], v[142:143], v[12:13]
	v_pk_mul_f32 v[46:47], v[46:47], v[20:21] op_sel_hi:[1,0]
	v_pk_mul_f32 v[50:51], v[50:51], v[20:21] op_sel_hi:[1,0]
	v_cvt_pk_fp8_f32 v54, v46, v47 op_sel:[0,0,1]
	v_cvt_pk_fp8_f32 v55, v50, v51 op_sel:[0,0,1]
	s_mov_b32 s31, 0x50000
	v_add_co_u32_e32 v48, vcc, s31, v34
	v_mul_f32_e32 v18, 0x41800000, v21
	s_nop 0
	v_addc_co_u32_e32 v49, vcc, 0, v35, vcc
	v_pk_add_f32 v[14:15], v[132:133], v[14:15]
	v_pk_add_f32 v[10:11], v[124:125], v[10:11]
	global_store_dwordx2 v[48:49], v[54:55], off
	v_pk_mul_f32 v[14:15], v[14:15], v[18:19] op_sel_hi:[1,0]
	v_pk_mul_f32 v[10:11], v[10:11], v[18:19] op_sel_hi:[1,0]
	v_mov_b32_e32 v48, v99
	v_mov_b32_e32 v49, v99
	v_cvt_pk_fp8_f32 v48, v14, v15
	v_cvt_pk_fp8_f32 v49, v10, v11
	v_pk_add_f32 v[16:17], v[134:135], v[16:17]
	v_pk_add_f32 v[12:13], v[126:127], v[12:13]
	v_pk_mul_f32 v[16:17], v[16:17], v[18:19] op_sel_hi:[1,0]
	v_pk_mul_f32 v[12:13], v[12:13], v[18:19] op_sel_hi:[1,0]
	v_cvt_pk_fp8_f32 v48, v16, v17 op_sel:[0,0,1]
	v_cvt_pk_fp8_f32 v49, v12, v13 op_sel:[0,0,1]
	s_mov_b32 s31, 0x58000
	v_add_co_u32_e32 v12, vcc, s31, v34
	v_pk_add_f32 v[14:15], v[136:137], v[6:7]
	s_nop 0
	v_addc_co_u32_e32 v13, vcc, 0, v35, vcc
	global_store_dwordx2 v[12:13], v[48:49], off
	v_pk_add_f32 v[12:13], v[138:139], v[8:9]
	v_pk_add_f32 v[16:17], v[130:131], v[4:5]
	v_pk_add_f32 v[48:49], v[128:129], v[2:3]
	v_pk_mul_f32 v[12:13], v[12:13], v[32:33] op_sel_hi:[1,0]
	v_pk_mul_f32 v[14:15], v[14:15], v[32:33] op_sel_hi:[1,0]
	v_pk_mul_f32 v[16:17], v[16:17], v[32:33] op_sel_hi:[1,0]
	v_pk_mul_f32 v[32:33], v[48:49], v[32:33] op_sel_hi:[1,0]
	v_mov_b32_e32 v48, v99
	v_mov_b32_e32 v49, v99
	v_cvt_pk_fp8_f32 v48, v14, v15
	v_cvt_pk_fp8_f32 v49, v32, v33
	v_pk_add_f32 v[14:15], v[120:121], v[6:7]
	v_pk_add_f32 v[32:33], v[116:117], v[2:3]
	v_cvt_pk_fp8_f32 v48, v12, v13 op_sel:[0,0,1]
	v_cvt_pk_fp8_f32 v49, v16, v17 op_sel:[0,0,1]
	v_pk_add_f32 v[12:13], v[122:123], v[8:9]
	v_pk_add_f32 v[16:17], v[118:119], v[4:5]
	v_pk_mul_f32 v[12:13], v[12:13], v[30:31] op_sel_hi:[1,0]
	v_pk_mul_f32 v[14:15], v[14:15], v[30:31] op_sel_hi:[1,0]
	v_pk_mul_f32 v[16:17], v[16:17], v[30:31] op_sel_hi:[1,0]
	v_pk_mul_f32 v[30:31], v[32:33], v[30:31] op_sel_hi:[1,0]
	v_mov_b32_e32 v32, v99
	v_mov_b32_e32 v33, v99
	v_cvt_pk_fp8_f32 v32, v14, v15
	v_cvt_pk_fp8_f32 v33, v30, v31
	v_pk_add_f32 v[14:15], v[112:113], v[6:7]
	v_pk_add_f32 v[30:31], v[108:109], v[2:3]
	v_cvt_pk_fp8_f32 v32, v12, v13 op_sel:[0,0,1]
	v_cvt_pk_fp8_f32 v33, v16, v17 op_sel:[0,0,1]
	v_pk_add_f32 v[12:13], v[114:115], v[8:9]
	v_pk_add_f32 v[16:17], v[110:111], v[4:5]
	v_pk_mul_f32 v[12:13], v[12:13], v[28:29] op_sel_hi:[1,0]
	v_pk_mul_f32 v[14:15], v[14:15], v[28:29] op_sel_hi:[1,0]
	v_pk_mul_f32 v[16:17], v[16:17], v[28:29] op_sel_hi:[1,0]
	v_pk_mul_f32 v[28:29], v[30:31], v[28:29] op_sel_hi:[1,0]
	v_mov_b32_e32 v30, v99
	v_mov_b32_e32 v31, v99
	v_cvt_pk_fp8_f32 v30, v14, v15
	v_cvt_pk_fp8_f32 v31, v28, v29
	v_pk_add_f32 v[14:15], v[104:105], v[6:7]
	v_pk_add_f32 v[28:29], v[100:101], v[2:3]
	v_cvt_pk_fp8_f32 v30, v12, v13 op_sel:[0,0,1]
	v_cvt_pk_fp8_f32 v31, v16, v17 op_sel:[0,0,1]
	v_pk_add_f32 v[12:13], v[106:107], v[8:9]
	v_pk_add_f32 v[16:17], v[102:103], v[4:5]
	v_pk_mul_f32 v[12:13], v[12:13], v[26:27] op_sel_hi:[1,0]
	v_pk_mul_f32 v[14:15], v[14:15], v[26:27] op_sel_hi:[1,0]
	v_pk_mul_f32 v[16:17], v[16:17], v[26:27] op_sel_hi:[1,0]
	v_pk_mul_f32 v[26:27], v[28:29], v[26:27] op_sel_hi:[1,0]
	v_mov_b32_e32 v28, v99
	v_mov_b32_e32 v29, v99
	v_cvt_pk_fp8_f32 v28, v14, v15
	v_cvt_pk_fp8_f32 v29, v26, v27
	v_pk_add_f32 v[14:15], v[94:95], v[6:7]
	v_pk_add_f32 v[26:27], v[90:91], v[2:3]
	v_cvt_pk_fp8_f32 v28, v12, v13 op_sel:[0,0,1]
	v_cvt_pk_fp8_f32 v29, v16, v17 op_sel:[0,0,1]
	v_pk_add_f32 v[12:13], v[96:97], v[8:9]
	v_pk_add_f32 v[16:17], v[92:93], v[4:5]
	v_pk_mul_f32 v[12:13], v[12:13], v[24:25] op_sel_hi:[1,0]
	v_pk_mul_f32 v[14:15], v[14:15], v[24:25] op_sel_hi:[1,0]
	v_pk_mul_f32 v[16:17], v[16:17], v[24:25] op_sel_hi:[1,0]
	v_pk_mul_f32 v[24:25], v[26:27], v[24:25] op_sel_hi:[1,0]
	v_mov_b32_e32 v26, v99
	v_mov_b32_e32 v27, v99
	v_cvt_pk_fp8_f32 v26, v14, v15
	v_cvt_pk_fp8_f32 v27, v24, v25
	v_pk_add_f32 v[14:15], v[86:87], v[6:7]
	v_pk_add_f32 v[24:25], v[82:83], v[2:3]
	v_cvt_pk_fp8_f32 v26, v12, v13 op_sel:[0,0,1]
	v_cvt_pk_fp8_f32 v27, v16, v17 op_sel:[0,0,1]
	v_pk_add_f32 v[12:13], v[88:89], v[8:9]
	v_pk_add_f32 v[16:17], v[84:85], v[4:5]
	v_pk_mul_f32 v[12:13], v[12:13], v[22:23] op_sel_hi:[1,0]
	v_pk_mul_f32 v[14:15], v[14:15], v[22:23] op_sel_hi:[1,0]
	v_pk_mul_f32 v[16:17], v[16:17], v[22:23] op_sel_hi:[1,0]
	v_pk_mul_f32 v[22:23], v[24:25], v[22:23] op_sel_hi:[1,0]
	v_mov_b32_e32 v24, v99
	v_mov_b32_e32 v25, v99
	v_cvt_pk_fp8_f32 v24, v14, v15
	v_cvt_pk_fp8_f32 v25, v22, v23
	v_pk_add_f32 v[14:15], v[78:79], v[6:7]
	v_pk_add_f32 v[22:23], v[74:75], v[2:3]
	v_cvt_pk_fp8_f32 v24, v12, v13 op_sel:[0,0,1]
	v_cvt_pk_fp8_f32 v25, v16, v17 op_sel:[0,0,1]
	v_pk_add_f32 v[12:13], v[80:81], v[8:9]
	v_pk_add_f32 v[16:17], v[76:77], v[4:5]
	v_pk_mul_f32 v[12:13], v[12:13], v[20:21] op_sel_hi:[1,0]
	v_pk_mul_f32 v[14:15], v[14:15], v[20:21] op_sel_hi:[1,0]
	v_pk_mul_f32 v[16:17], v[16:17], v[20:21] op_sel_hi:[1,0]
	v_pk_mul_f32 v[20:21], v[22:23], v[20:21] op_sel_hi:[1,0]
	v_mov_b32_e32 v22, v99
	v_cvt_pk_fp8_f32 v22, v14, v15
	v_pk_add_f32 v[6:7], v[70:71], v[6:7]
	v_pk_add_f32 v[2:3], v[66:67], v[2:3]
	v_mov_b32_e32 v23, v99
	v_cvt_pk_fp8_f32 v22, v12, v13 op_sel:[0,0,1]
	v_pk_mul_f32 v[6:7], v[6:7], v[18:19] op_sel_hi:[1,0]
	v_pk_mul_f32 v[2:3], v[2:3], v[18:19] op_sel_hi:[1,0]
	v_mov_b32_e32 v12, v99
	v_mov_b32_e32 v13, v99
	v_cvt_pk_fp8_f32 v23, v20, v21
	v_cvt_pk_fp8_f32 v12, v6, v7
	v_cvt_pk_fp8_f32 v13, v2, v3
	v_lshl_add_u64 v[36:37], v[34:35], 0, s[42:43]
	s_mov_b64 s[42:43], 0x10000
	v_lshl_add_u64 v[38:39], v[34:35], 0, s[42:43]
	s_mov_b64 s[42:43], 0x18000
	v_pk_add_f32 v[8:9], v[72:73], v[8:9]
	v_pk_add_f32 v[4:5], v[68:69], v[4:5]
	v_lshl_add_u64 v[40:41], v[34:35], 0, s[42:43]
	s_mov_b64 s[42:43], 0x40000
	v_pk_mul_f32 v[8:9], v[8:9], v[18:19] op_sel_hi:[1,0]
	v_pk_mul_f32 v[4:5], v[4:5], v[18:19] op_sel_hi:[1,0]
	v_lshl_add_u64 v[42:43], v[34:35], 0, s[42:43]
	s_mov_b64 s[42:43], 0x48000
	v_cvt_pk_fp8_f32 v23, v16, v17 op_sel:[0,0,1]
	v_cvt_pk_fp8_f32 v12, v8, v9 op_sel:[0,0,1]
	v_cvt_pk_fp8_f32 v13, v4, v5 op_sel:[0,0,1]
	v_lshl_add_u64 v[44:45], v[34:35], 0, s[42:43]
	s_mov_b64 s[42:43], 0x50000
	v_lshl_add_u64 v[46:47], v[34:35], 0, s[42:43]
	s_mov_b64 s[42:43], 0x58000
	v_lshl_add_u64 v[10:11], v[34:35], 0, s[42:43]
	s_mov_b64 s[42:43], -1
	s_andn2_b64 vcc, exec, s[8:9]
	global_store_dwordx2 v[34:35], v[48:49], off offset:128
	global_store_dwordx2 v[36:37], v[32:33], off offset:128
	global_store_dwordx2 v[38:39], v[30:31], off offset:128
	global_store_dwordx2 v[40:41], v[28:29], off offset:128
	global_store_dwordx2 v[42:43], v[26:27], off offset:128
	global_store_dwordx2 v[44:45], v[24:25], off offset:128
	global_store_dwordx2 v[46:47], v[22:23], off offset:128
	global_store_dwordx2 v[10:11], v[12:13], off offset:128
	s_cbranch_vccnz .LBB0_1501
	s_andn2_b64 vcc, exec, s[4:5]
	s_cbranch_vccnz .LBB0_1500
	s_barrier
	s_branch .LBB0_1500
